# conv quotas P2:20 P3:12 (was 16/16)
# baseline (speedup 1.0000x reference)
.LBB0_165:
	s_cmp_lt_i32 s88, 3
	s_cselect_b64 s[6:7], -1, 0
	v_writelane_b32 v252, s94, 5
	s_bfe_u32 s70, s94, 0x20003
	s_and_b64 s[2:3], s[6:7], s[2:3]
	v_writelane_b32 v252, s86, 6
	s_andn2_b64 vcc, exec, s[2:3]
	s_mov_b32 s61, 0
	v_writelane_b32 v252, s70, 7
	v_writelane_b32 v252, s87, 8
	s_cbranch_vccnz .LBB0_214
	s_cmp_lg_u32 s70, 0
	s_cbranch_scc1 .LBB0_171
	v_writelane_b32 v255, 1, 5
	v_writelane_b32 v255, 20, 6
	s_branch .Lmy_cvgu

.LBB0_185:
	s_lshl_b32 s39, s10, 10
	s_and_b32 s39, s39, 0x400
	v_add_u32_e32 v130, s39, v164
	ds_read_b128 v[142:145], v130
	ds_read_b128 v[138:141], v130 offset:16
	ds_read_b128 v[134:137], v130 offset:512
	ds_read_b128 v[130:133], v130 offset:528
	s_and_b32 s40, s89, -4
	s_cmp_eq_u32 s40, 12
	v_lshl_or_b32 v160, s89, 8, v181
	v_lshl_add_u32 v192, s88, 8, v163
	s_cselect_b64 vcc, -1, 0
	v_ashrrev_i32_e32 v161, 31, v160
	v_mov_b64_e32 v[158:159], s[26:27]
	v_cndmask_b32_e32 v150, 1.0, v183, vcc
	v_mad_i64_i32 v[188:189], s[40:41], v192, s76, v[158:159]
	v_lshlrev_b64 v[160:161], 1, v[160:161]
	s_waitcnt lgkmcnt(0)
	v_pk_add_f32 v[128:129], v[128:129], v[144:145]
	v_pk_add_f32 v[126:127], v[126:127], v[142:143]
	v_pk_add_f32 v[124:125], v[124:125], v[140:141]
	v_pk_add_f32 v[122:123], v[122:123], v[138:139]
	v_lshl_add_u64 v[188:189], v[188:189], 0, v[160:161]
	v_pk_mul_f32 v[128:129], v[150:151], v[128:129] op_sel_hi:[0,1]
	v_pk_mul_f32 v[126:127], v[150:151], v[126:127] op_sel_hi:[0,1]
	v_pk_mul_f32 v[190:191], v[150:151], v[124:125] op_sel_hi:[0,1]
	v_pk_mul_f32 v[124:125], v[150:151], v[122:123] op_sel_hi:[0,1]
	v_cvt_pk_bf16_f32 v122, v126, v127
	v_cvt_pk_bf16_f32 v123, v128, v129
	v_pk_add_f32 v[118:119], v[118:119], v[134:135]
	v_pk_add_f32 v[112:113], v[112:113], v[132:133]
	v_pk_add_f32 v[110:111], v[110:111], v[130:131]
	v_cvt_pk_bf16_f32 v124, v124, v125
	v_cvt_pk_bf16_f32 v125, v190, v191
	global_store_dwordx4 v[188:189], v[122:125], off
	v_pk_add_f32 v[120:121], v[120:121], v[136:137]
	v_pk_mul_f32 v[118:119], v[150:151], v[118:119] op_sel_hi:[0,1]
	v_pk_mul_f32 v[122:123], v[150:151], v[112:113] op_sel_hi:[0,1]
	v_pk_mul_f32 v[112:113], v[150:151], v[110:111] op_sel_hi:[0,1]
	v_cvt_pk_bf16_f32 v110, v118, v119
	v_pk_mul_f32 v[120:121], v[150:151], v[120:121] op_sel_hi:[0,1]
	v_cvt_pk_bf16_f32 v111, v120, v121
	v_cvt_pk_bf16_f32 v112, v112, v113
	v_cvt_pk_bf16_f32 v113, v122, v123
	global_store_dwordx4 v[188:189], v[110:113], off offset:256
	v_pk_add_f32 v[114:115], v[114:115], v[142:143]
	v_pk_add_f32 v[108:109], v[108:109], v[140:141]
	v_or_b32_e32 v110, 16, v192
	v_mad_i64_i32 v[110:111], s[40:41], v110, s76, v[158:159]
	v_pk_add_f32 v[112:113], v[116:117], v[144:145]
	v_pk_add_f32 v[106:107], v[106:107], v[138:139]
	v_lshl_add_u64 v[110:111], v[110:111], 0, v[160:161]
	v_pk_mul_f32 v[112:113], v[150:151], v[112:113] op_sel_hi:[0,1]
	v_pk_mul_f32 v[114:115], v[150:151], v[114:115] op_sel_hi:[0,1]
	v_pk_mul_f32 v[116:117], v[150:151], v[108:109] op_sel_hi:[0,1]
	v_pk_mul_f32 v[108:109], v[150:151], v[106:107] op_sel_hi:[0,1]
	v_cvt_pk_bf16_f32 v106, v114, v115
	v_cvt_pk_bf16_f32 v107, v112, v113
	v_pk_add_f32 v[102:103], v[102:103], v[134:135]
	v_pk_add_f32 v[96:97], v[96:97], v[132:133]
	v_pk_add_f32 v[94:95], v[94:95], v[130:131]
	v_cvt_pk_bf16_f32 v108, v108, v109
	v_cvt_pk_bf16_f32 v109, v116, v117
	global_store_dwordx4 v[110:111], v[106:109], off
	v_pk_add_f32 v[104:105], v[104:105], v[136:137]
	v_pk_mul_f32 v[102:103], v[150:151], v[102:103] op_sel_hi:[0,1]
	v_pk_mul_f32 v[106:107], v[150:151], v[96:97] op_sel_hi:[0,1]
	v_pk_mul_f32 v[96:97], v[150:151], v[94:95] op_sel_hi:[0,1]
	v_cvt_pk_bf16_f32 v94, v102, v103
	v_pk_mul_f32 v[104:105], v[150:151], v[104:105] op_sel_hi:[0,1]
	v_cvt_pk_bf16_f32 v95, v104, v105
	v_cvt_pk_bf16_f32 v96, v96, v97
	v_cvt_pk_bf16_f32 v97, v106, v107
	global_store_dwordx4 v[110:111], v[94:97], off offset:256
	v_pk_add_f32 v[98:99], v[98:99], v[142:143]
	v_pk_add_f32 v[92:93], v[92:93], v[140:141]
	v_or_b32_e32 v94, 32, v192
	v_mad_i64_i32 v[94:95], s[40:41], v94, s76, v[158:159]
	v_pk_add_f32 v[96:97], v[100:101], v[144:145]
	v_pk_add_f32 v[90:91], v[90:91], v[138:139]
	v_lshl_add_u64 v[94:95], v[94:95], 0, v[160:161]
	v_pk_mul_f32 v[96:97], v[150:151], v[96:97] op_sel_hi:[0,1]
	v_pk_mul_f32 v[98:99], v[150:151], v[98:99] op_sel_hi:[0,1]
	v_pk_mul_f32 v[100:101], v[150:151], v[92:93] op_sel_hi:[0,1]
	v_pk_mul_f32 v[92:93], v[150:151], v[90:91] op_sel_hi:[0,1]
	v_cvt_pk_bf16_f32 v90, v98, v99
	v_cvt_pk_bf16_f32 v91, v96, v97
	v_pk_add_f32 v[86:87], v[86:87], v[134:135]
	v_pk_add_f32 v[80:81], v[80:81], v[132:133]
	v_pk_add_f32 v[78:79], v[78:79], v[130:131]
	v_cvt_pk_bf16_f32 v92, v92, v93
	v_cvt_pk_bf16_f32 v93, v100, v101
	global_store_dwordx4 v[94:95], v[90:93], off
	v_pk_add_f32 v[88:89], v[88:89], v[136:137]
	v_pk_mul_f32 v[86:87], v[150:151], v[86:87] op_sel_hi:[0,1]
	v_pk_mul_f32 v[90:91], v[150:151], v[80:81] op_sel_hi:[0,1]
	v_pk_mul_f32 v[80:81], v[150:151], v[78:79] op_sel_hi:[0,1]
	v_cvt_pk_bf16_f32 v78, v86, v87
	v_pk_mul_f32 v[88:89], v[150:151], v[88:89] op_sel_hi:[0,1]
	v_cvt_pk_bf16_f32 v79, v88, v89
	v_cvt_pk_bf16_f32 v80, v80, v81
	v_cvt_pk_bf16_f32 v81, v90, v91
	global_store_dwordx4 v[94:95], v[78:81], off offset:256
	v_pk_add_f32 v[82:83], v[82:83], v[142:143]
	v_pk_add_f32 v[76:77], v[76:77], v[140:141]
	v_or_b32_e32 v78, 48, v192
	v_mad_i64_i32 v[78:79], s[40:41], v78, s76, v[158:159]
	v_pk_add_f32 v[80:81], v[84:85], v[144:145]
	v_pk_add_f32 v[74:75], v[74:75], v[138:139]
	v_lshl_add_u64 v[78:79], v[78:79], 0, v[160:161]
	v_pk_mul_f32 v[80:81], v[150:151], v[80:81] op_sel_hi:[0,1]
	v_pk_mul_f32 v[82:83], v[150:151], v[82:83] op_sel_hi:[0,1]
	v_pk_mul_f32 v[84:85], v[150:151], v[76:77] op_sel_hi:[0,1]
	v_pk_mul_f32 v[76:77], v[150:151], v[74:75] op_sel_hi:[0,1]
	v_cvt_pk_bf16_f32 v74, v82, v83
	v_cvt_pk_bf16_f32 v75, v80, v81
	v_pk_add_f32 v[70:71], v[70:71], v[134:135]
	v_pk_add_f32 v[68:69], v[68:69], v[132:133]
	v_pk_add_f32 v[66:67], v[66:67], v[130:131]
	v_cvt_pk_bf16_f32 v76, v76, v77
	v_cvt_pk_bf16_f32 v77, v84, v85
	global_store_dwordx4 v[78:79], v[74:77], off
	v_pk_add_f32 v[72:73], v[72:73], v[136:137]
	v_pk_mul_f32 v[70:71], v[150:151], v[70:71] op_sel_hi:[0,1]
	v_pk_mul_f32 v[74:75], v[150:151], v[68:69] op_sel_hi:[0,1]
	v_pk_mul_f32 v[68:69], v[150:151], v[66:67] op_sel_hi:[0,1]
	v_cvt_pk_bf16_f32 v66, v70, v71
	v_pk_mul_f32 v[72:73], v[150:151], v[72:73] op_sel_hi:[0,1]
	v_cvt_pk_bf16_f32 v67, v72, v73
	v_cvt_pk_bf16_f32 v68, v68, v69
	v_cvt_pk_bf16_f32 v69, v74, v75
	global_store_dwordx4 v[78:79], v[66:69], off offset:256
	v_pk_add_f32 v[64:65], v[64:65], v[144:145]
	v_pk_add_f32 v[62:63], v[62:63], v[142:143]
	v_add_u32_e32 v66, 0x80, v192
	v_mad_i64_i32 v[66:67], s[40:41], v66, s76, v[158:159]
	v_pk_add_f32 v[60:61], v[60:61], v[140:141]
	v_pk_add_f32 v[58:59], v[58:59], v[138:139]
	v_lshl_add_u64 v[66:67], v[66:67], 0, v[160:161]
	v_pk_mul_f32 v[64:65], v[150:151], v[64:65] op_sel_hi:[0,1]
	v_pk_mul_f32 v[62:63], v[150:151], v[62:63] op_sel_hi:[0,1]
	v_pk_mul_f32 v[68:69], v[150:151], v[60:61] op_sel_hi:[0,1]
	v_pk_mul_f32 v[60:61], v[150:151], v[58:59] op_sel_hi:[0,1]
	v_cvt_pk_bf16_f32 v58, v62, v63
	v_cvt_pk_bf16_f32 v59, v64, v65
	v_pk_add_f32 v[54:55], v[54:55], v[134:135]
	v_pk_add_f32 v[48:49], v[48:49], v[132:133]
	v_pk_add_f32 v[46:47], v[46:47], v[130:131]
	v_cvt_pk_bf16_f32 v60, v60, v61
	v_cvt_pk_bf16_f32 v61, v68, v69
	global_store_dwordx4 v[66:67], v[58:61], off
	v_pk_add_f32 v[56:57], v[56:57], v[136:137]
	v_pk_mul_f32 v[54:55], v[150:151], v[54:55] op_sel_hi:[0,1]
	v_pk_mul_f32 v[58:59], v[150:151], v[48:49] op_sel_hi:[0,1]
	v_pk_mul_f32 v[48:49], v[150:151], v[46:47] op_sel_hi:[0,1]
	v_cvt_pk_bf16_f32 v46, v54, v55
	v_pk_mul_f32 v[56:57], v[150:151], v[56:57] op_sel_hi:[0,1]
	v_cvt_pk_bf16_f32 v47, v56, v57
	v_cvt_pk_bf16_f32 v48, v48, v49
	v_cvt_pk_bf16_f32 v49, v58, v59
	global_store_dwordx4 v[66:67], v[46:49], off offset:256
	v_pk_add_f32 v[50:51], v[50:51], v[142:143]
	v_pk_add_f32 v[44:45], v[44:45], v[140:141]
	v_add_u32_e32 v46, 0x90, v192
	v_mad_i64_i32 v[46:47], s[40:41], v46, s76, v[158:159]
	v_pk_add_f32 v[48:49], v[52:53], v[144:145]
	v_pk_add_f32 v[42:43], v[42:43], v[138:139]
	v_lshl_add_u64 v[46:47], v[46:47], 0, v[160:161]
	v_pk_mul_f32 v[48:49], v[150:151], v[48:49] op_sel_hi:[0,1]
	v_pk_mul_f32 v[50:51], v[150:151], v[50:51] op_sel_hi:[0,1]
	v_pk_mul_f32 v[52:53], v[150:151], v[44:45] op_sel_hi:[0,1]
	v_pk_mul_f32 v[44:45], v[150:151], v[42:43] op_sel_hi:[0,1]
	v_cvt_pk_bf16_f32 v42, v50, v51
	v_cvt_pk_bf16_f32 v43, v48, v49
	v_pk_add_f32 v[30:31], v[30:31], v[134:135]
	v_pk_add_f32 v[16:17], v[16:17], v[132:133]
	v_pk_add_f32 v[14:15], v[14:15], v[130:131]
	v_cvt_pk_bf16_f32 v44, v44, v45
	v_cvt_pk_bf16_f32 v45, v52, v53
	global_store_dwordx4 v[46:47], v[42:45], off
	v_pk_add_f32 v[32:33], v[32:33], v[136:137]
	v_pk_mul_f32 v[30:31], v[150:151], v[30:31] op_sel_hi:[0,1]
	v_pk_mul_f32 v[42:43], v[150:151], v[16:17] op_sel_hi:[0,1]
	v_pk_mul_f32 v[16:17], v[150:151], v[14:15] op_sel_hi:[0,1]
	v_cvt_pk_bf16_f32 v14, v30, v31
	v_pk_mul_f32 v[32:33], v[150:151], v[32:33] op_sel_hi:[0,1]
	v_cvt_pk_bf16_f32 v15, v32, v33
	v_cvt_pk_bf16_f32 v16, v16, v17
	v_cvt_pk_bf16_f32 v17, v42, v43
	global_store_dwordx4 v[46:47], v[14:17], off offset:256
	v_pk_add_f32 v[12:13], v[12:13], v[140:141]
	v_pk_add_f32 v[10:11], v[10:11], v[138:139]
	v_add_u32_e32 v14, 0xa0, v192
	v_mad_i64_i32 v[14:15], s[40:41], v14, s76, v[158:159]
	v_pk_add_f32 v[16:17], v[20:21], v[144:145]
	v_pk_add_f32 v[18:19], v[18:19], v[142:143]
	v_pk_mul_f32 v[20:21], v[150:151], v[12:13] op_sel_hi:[0,1]
	v_pk_mul_f32 v[12:13], v[150:151], v[10:11] op_sel_hi:[0,1]
	v_lshl_add_u64 v[14:15], v[14:15], 0, v[160:161]
	v_pk_mul_f32 v[16:17], v[150:151], v[16:17] op_sel_hi:[0,1]
	v_pk_mul_f32 v[18:19], v[150:151], v[18:19] op_sel_hi:[0,1]
	v_cvt_pk_bf16_f32 v10, v18, v19
	v_cvt_pk_bf16_f32 v11, v16, v17
	v_cvt_pk_bf16_f32 v12, v12, v13
	v_cvt_pk_bf16_f32 v13, v20, v21
	global_store_dwordx4 v[14:15], v[10:13], off
	v_pk_add_f32 v[18:19], v[34:35], v[130:131]
	v_pk_add_f32 v[4:5], v[4:5], v[140:141]
	v_pk_add_f32 v[10:11], v[40:41], v[136:137]
	v_pk_add_f32 v[12:13], v[38:39], v[134:135]
	v_pk_mul_f32 v[16:17], v[150:151], v[10:11] op_sel_hi:[0,1]
	v_pk_mul_f32 v[10:11], v[150:151], v[12:13] op_sel_hi:[0,1]
	v_pk_add_f32 v[12:13], v[36:37], v[132:133]
	v_cvt_pk_bf16_f32 v10, v10, v11
	v_cvt_pk_bf16_f32 v11, v16, v17
	v_pk_add_f32 v[2:3], v[2:3], v[138:139]
	v_pk_mul_f32 v[20:21], v[150:151], v[12:13] op_sel_hi:[0,1]
	v_pk_mul_f32 v[12:13], v[150:151], v[18:19] op_sel_hi:[0,1]
	v_cvt_pk_bf16_f32 v12, v12, v13
	v_cvt_pk_bf16_f32 v13, v20, v21
	global_store_dwordx4 v[14:15], v[10:13], off offset:256
	v_pk_add_f32 v[8:9], v[8:9], v[144:145]
	v_pk_add_f32 v[6:7], v[6:7], v[142:143]
	v_add_u32_e32 v10, 0xb0, v192
	v_mad_i64_i32 v[10:11], s[40:41], v10, s76, v[158:159]
	v_pk_mul_f32 v[12:13], v[150:151], v[4:5] op_sel_hi:[0,1]
	v_pk_mul_f32 v[4:5], v[150:151], v[2:3] op_sel_hi:[0,1]
	v_lshl_add_u64 v[10:11], v[10:11], 0, v[160:161]
	v_pk_mul_f32 v[8:9], v[150:151], v[8:9] op_sel_hi:[0,1]
	v_pk_mul_f32 v[6:7], v[150:151], v[6:7] op_sel_hi:[0,1]
	v_cvt_pk_bf16_f32 v2, v6, v7
	v_cvt_pk_bf16_f32 v3, v8, v9
	v_cvt_pk_bf16_f32 v4, v4, v5
	v_cvt_pk_bf16_f32 v5, v12, v13
	global_store_dwordx4 v[10:11], v[2:5], off
	v_pk_add_f32 v[8:9], v[22:23], v[130:131]
	s_cmp_lg_u32 s10, s52
	v_pk_add_f32 v[2:3], v[28:29], v[136:137]
	v_pk_add_f32 v[4:5], v[26:27], v[134:135]
	v_pk_mul_f32 v[6:7], v[150:151], v[2:3] op_sel_hi:[0,1]
	v_pk_mul_f32 v[2:3], v[150:151], v[4:5] op_sel_hi:[0,1]
	v_pk_add_f32 v[4:5], v[24:25], v[132:133]
	v_cvt_pk_bf16_f32 v2, v2, v3
	v_cvt_pk_bf16_f32 v3, v6, v7
	s_nop 0
	v_pk_mul_f32 v[12:13], v[150:151], v[4:5] op_sel_hi:[0,1]
	v_pk_mul_f32 v[4:5], v[150:151], v[8:9] op_sel_hi:[0,1]
	v_cvt_pk_bf16_f32 v4, v4, v5
	v_cvt_pk_bf16_f32 v5, v12, v13
	global_store_dwordx4 v[10:11], v[2:5], off offset:256
	s_cbranch_scc1 .LBB0_192
	s_nop 0
	v_mov_b32_e32 v2, v0
	s_mov_b32 s40, 15
	s_andn2_b64 vcc, exec, s[14:15]
	s_cbranch_vccnz .LBB0_192
	v_writelane_b32 v255, 2, 5
	v_writelane_b32 v255, 20, 6
	s_branch .Lmy_cvgu

.LBB0_204:
	s_cmp_lg_u32 s70, 3
	s_cbranch_scc1 .LBB0_214
	v_writelane_b32 v255, 3, 5
	v_writelane_b32 v255, 20, 6
	s_branch .Lmy_cvgu

.LBB0_264:
	s_cmp_lt_i32 s88, 4
	s_cselect_b64 s[4:5], -1, 0
	s_and_b64 s[2:3], s[4:5], s[2:3]
	s_andn2_b64 vcc, exec, s[2:3]
	s_cbranch_vccnz .LBB0_526
	s_cmp_lg_u32 s70, 0
	s_mov_b32 s3, 0
	v_writelane_b32 v252, s4, 10
	s_nop 1
	v_writelane_b32 v252, s5, 11
	s_cbranch_scc1 .LBB0_276
	v_writelane_b32 v255, 4, 5
	v_writelane_b32 v255, 12, 6
	s_branch .Lmy_cvgu

.LBB0_368:
	v_add_f32_e32 v68, v52, v53
	v_add_f32_e32 v68, v54, v68
	v_add_f32_e32 v68, v55, v68
	v_add_f32_e32 v68, v56, v68
	v_add_f32_e32 v68, v57, v68
	v_add_f32_e32 v68, v58, v68
	v_add_f32_e32 v68, v59, v68
	v_add_f32_e32 v68, v60, v68
	v_add_f32_e32 v68, v61, v68
	v_add_f32_e32 v68, v62, v68
	v_add_f32_e32 v68, v63, v68
	v_add_f32_e32 v68, v64, v68
	v_add_f32_e32 v68, v65, v68
	v_add_f32_e32 v68, v66, v68
	v_add_f32_e32 v68, v67, v68
	v_add_f32_e32 v68, v36, v68
	v_add_f32_e32 v68, v37, v68
	v_add_f32_e32 v68, v38, v68
	v_add_f32_e32 v68, v39, v68
	v_add_f32_e32 v68, v40, v68
	v_add_f32_e32 v68, v41, v68
	v_add_f32_e32 v68, v42, v68
	v_add_f32_e32 v68, v43, v68
	v_add_f32_e32 v68, v44, v68
	v_add_f32_e32 v68, v45, v68
	v_add_f32_e32 v68, v46, v68
	v_add_f32_e32 v68, v47, v68
	v_add_f32_e32 v68, v48, v68
	v_add_f32_e32 v68, v49, v68
	v_add_f32_e32 v68, v50, v68
	v_add_f32_e32 v68, v51, v68
	v_add_f32_e32 v2, v2, v68
	v_cvt_pk_bf16_f32 v36, v36, v37
	v_cvt_pk_bf16_f32 v52, v52, v53
	v_cvt_pk_bf16_f32 v53, v54, v55
	v_cvt_pk_bf16_f32 v54, v56, v57
	v_cvt_pk_bf16_f32 v55, v58, v59
	v_cvt_pk_bf16_f32 v56, v60, v61
	v_cvt_pk_bf16_f32 v57, v62, v63
	v_cvt_pk_bf16_f32 v58, v64, v65
	v_cvt_pk_bf16_f32 v59, v66, v67
	v_cvt_pk_bf16_f32 v37, v38, v39
	v_cvt_pk_bf16_f32 v38, v40, v41
	v_cvt_pk_bf16_f32 v39, v42, v43
	v_cvt_pk_bf16_f32 v40, v44, v45
	v_cvt_pk_bf16_f32 v41, v46, v47
	v_cvt_pk_bf16_f32 v42, v48, v49
	v_cvt_pk_bf16_f32 v43, v50, v51
	s_cmp_lg_u32 0, -1
	s_cselect_b32 s2, 0, 0
	s_addk_i32 s2, 0x6000
	v_add3_u32 v44, v204, s2, v203
	v_add3_u32 v72, v44, v205, s17
	ds_read_b64_tr_b16 v[44:45],v72 offset:0
	ds_read_b64_tr_b16 v[46:47],v72 offset:512
	ds_read_b64_tr_b16 v[48:49],v72 offset:1024
	ds_read_b64_tr_b16 v[50:51],v72 offset:1536
	ds_read_b64_tr_b16 v[60:61],v72 offset:2048
	ds_read_b64_tr_b16 v[62:63],v72 offset:2560
	ds_read_b64_tr_b16 v[64:65],v72 offset:3072
	ds_read_b64_tr_b16 v[66:67],v72 offset:3584
	s_waitcnt lgkmcnt(0)
	s_nop 0
	v_mfma_f32_32x32x16_bf16 v[20:35], v[52:55], v[44:47], v[20:35]
	ds_read_b64_tr_b16 v[44:45],v72 offset:4096
	ds_read_b64_tr_b16 v[46:47],v72 offset:4608
	v_mfma_f32_32x32x16_bf16 v[20:35], v[56:59], v[48:51], v[20:35]
	ds_read_b64_tr_b16 v[48:49],v72 offset:5120
	ds_read_b64_tr_b16 v[50:51],v72 offset:5632
	v_mfma_f32_32x32x16_bf16 v[20:35], v[36:39], v[60:63], v[20:35]
	ds_read_b64_tr_b16 v[60:61],v72 offset:6144
	ds_read_b64_tr_b16 v[62:63],v72 offset:6656
	ds_read_b64_tr_b16 v[68:69],v72 offset:7168
	ds_read_b64_tr_b16 v[70:71],v72 offset:7680
	s_waitcnt lgkmcnt(0)
	v_mfma_f32_32x32x16_bf16 v[20:35], v[40:43], v[64:67], v[20:35]
	v_mfma_f32_32x32x16_bf16 v[4:19], v[52:55], v[44:47], v[4:19]
	v_cmp_gt_u32_e32 vcc, 32, v202
	v_mfma_f32_32x32x16_bf16 v[4:19], v[56:59], v[48:51], v[4:19]
	v_mfma_f32_32x32x16_bf16 v[4:19], v[36:39], v[60:63], v[4:19]
	v_mov_b32_e32 v36, v2
	s_nop 1
	v_permlane32_swap_b32_e32 v2, v36
	v_mfma_f32_32x32x16_bf16 v[4:19], v[40:43], v[68:71], v[4:19]
	s_and_saveexec_b64 s[2:3], vcc
	v_lshl_add_u32 v37, v202, 2, s21
	v_add_f32_e32 v2, v2, v36
	ds_write_b32 v37, v2 offset:49280
	s_or_b64 exec, exec, s[2:3]
	s_waitcnt lgkmcnt(0)
	ds_read_b128 v[36:39], v206 offset:49280
	ds_read_b128 v[40:43], v206 offset:49312
	v_mov_b32_e32 v52, v1
	s_lshl_b32 s2, s16, 12
	s_add_i32 s2, s2, 0
	s_waitcnt lgkmcnt(1)
	v_rcp_f32_e32 v2, v36
	v_rcp_f32_e32 v44, v37
	v_rcp_f32_e32 v45, v38
	v_rcp_f32_e32 v46, v39
	ds_read_b128 v[36:39], v206 offset:49344
	v_mul_f32_e32 v20, v20, v2
	s_waitcnt lgkmcnt(1)
	v_rcp_f32_e32 v47, v40
	v_rcp_f32_e32 v48, v41
	v_rcp_f32_e32 v49, v42
	v_rcp_f32_e32 v50, v43
	ds_read_b128 v[40:43], v206 offset:49376
	s_waitcnt lgkmcnt(1)
	v_rcp_f32_e32 v51, v36
	v_bfe_u32 v53, v20, 16, 1
	v_ashrrev_i32_e32 v36, 3, v52
	v_add3_u32 v20, v20, v53, s80
	v_lshlrev_b32_e32 v53, 7, v36
	v_lshlrev_b32_e32 v55, 1, v52
	v_mul_f32_e32 v2, v4, v2
	v_and_b32_e32 v54, 0xfffffe00, v53
	v_and_b32_e32 v55, 62, v55
	v_bfe_u32 v4, v2, 16, 1
	v_add3_u32 v54, s2, v54, v55
	v_add3_u32 v2, v2, v4, s80
	ds_write_b16_d16_hi v54, v2 offset:51264
	v_mul_f32_e32 v2, v21, v44
	v_bfe_u32 v4, v2, 16, 1
	v_add3_u32 v2, v2, v4, s80
	ds_write_b16_d16_hi v54, v2 offset:51328
	v_mul_f32_e32 v2, v5, v44
	v_bfe_u32 v4, v2, 16, 1
	v_add3_u32 v2, v2, v4, s80
	ds_write_b16_d16_hi v54, v2 offset:51392
	v_mul_f32_e32 v2, v22, v45
	v_bfe_u32 v4, v2, 16, 1
	v_add3_u32 v2, v2, v4, s80
	ds_write_b16_d16_hi v54, v2 offset:51456
	v_mul_f32_e32 v2, v6, v45
	v_bfe_u32 v4, v2, 16, 1
	v_add3_u32 v2, v2, v4, s80
	ds_write_b16_d16_hi v54, v2 offset:51520
	v_mul_f32_e32 v2, v23, v46
	v_bfe_u32 v4, v2, 16, 1
	v_add3_u32 v2, v2, v4, s80
	v_or_b32_e32 v4, 0x180, v53
	v_add3_u32 v4, s2, v4, v55
	ds_write_b16_d16_hi v54, v20 offset:51200
	ds_write_b16_d16_hi v4, v2 offset:51200
	v_mul_f32_e32 v2, v7, v46
	v_bfe_u32 v5, v2, 16, 1
	v_add3_u32 v2, v2, v5, s80
	ds_write_b16_d16_hi v4, v2 offset:51264
	v_mul_f32_e32 v2, v24, v47
	v_bfe_u32 v5, v2, 16, 1
	v_add3_u32 v2, v2, v5, s80
	ds_write_b16_d16_hi v54, v2 offset:52224
	v_mul_f32_e32 v2, v8, v47
	v_bfe_u32 v5, v2, 16, 1
	v_add3_u32 v2, v2, v5, s80
	ds_write_b16_d16_hi v54, v2 offset:52288
	v_mul_f32_e32 v2, v25, v48
	v_bfe_u32 v5, v2, 16, 1
	v_add3_u32 v2, v2, v5, s80
	ds_write_b16_d16_hi v54, v2 offset:52352
	v_mul_f32_e32 v2, v9, v48
	v_bfe_u32 v5, v2, 16, 1
	v_add3_u32 v2, v2, v5, s80
	ds_write_b16_d16_hi v54, v2 offset:52416
	v_mul_f32_e32 v2, v26, v49
	v_bfe_u32 v5, v2, 16, 1
	v_add3_u32 v2, v2, v5, s80
	ds_write_b16_d16_hi v54, v2 offset:52480
	v_mul_f32_e32 v2, v10, v49
	v_bfe_u32 v5, v2, 16, 1
	v_add3_u32 v2, v2, v5, s80
	ds_write_b16_d16_hi v54, v2 offset:52544
	v_mul_f32_e32 v2, v27, v50
	v_bfe_u32 v5, v2, 16, 1
	v_add3_u32 v2, v2, v5, s80
	ds_write_b16_d16_hi v4, v2 offset:52224
	v_mul_f32_e32 v2, v11, v50
	v_bfe_u32 v5, v2, 16, 1
	v_add3_u32 v2, v2, v5, s80
	ds_write_b16_d16_hi v4, v2 offset:52288
	v_mul_f32_e32 v2, v28, v51
	v_bfe_u32 v5, v2, 16, 1
	v_rcp_f32_e32 v37, v37
	v_add3_u32 v2, v2, v5, s80
	ds_write_b16_d16_hi v54, v2 offset:53248
	v_mul_f32_e32 v2, v12, v51
	v_bfe_u32 v5, v2, 16, 1
	v_add3_u32 v2, v2, v5, s80
	ds_write_b16_d16_hi v54, v2 offset:53312
	v_mul_f32_e32 v2, v29, v37
	v_bfe_u32 v5, v2, 16, 1
	v_rcp_f32_e32 v38, v38
	v_add3_u32 v2, v2, v5, s80
	ds_write_b16_d16_hi v54, v2 offset:53376
	v_mul_f32_e32 v2, v13, v37
	v_bfe_u32 v5, v2, 16, 1
	v_add3_u32 v2, v2, v5, s80
	ds_write_b16_d16_hi v54, v2 offset:53440
	v_mul_f32_e32 v2, v30, v38
	v_bfe_u32 v5, v2, 16, 1
	v_rcp_f32_e32 v39, v39
	v_add3_u32 v2, v2, v5, s80
	ds_write_b16_d16_hi v54, v2 offset:53504
	v_mul_f32_e32 v2, v14, v38
	v_bfe_u32 v5, v2, 16, 1
	v_add3_u32 v2, v2, v5, s80
	ds_write_b16_d16_hi v54, v2 offset:53568
	v_mul_f32_e32 v2, v31, v39
	v_bfe_u32 v5, v2, 16, 1
	s_waitcnt lgkmcnt(14)
	v_rcp_f32_e32 v40, v40
	v_add3_u32 v2, v2, v5, s80
	ds_write_b16_d16_hi v4, v2 offset:53248
	v_mul_f32_e32 v2, v15, v39
	v_bfe_u32 v5, v2, 16, 1
	v_add3_u32 v2, v2, v5, s80
	ds_write_b16_d16_hi v4, v2 offset:53312
	v_mul_f32_e32 v2, v32, v40
	v_bfe_u32 v5, v2, 16, 1
	v_rcp_f32_e32 v41, v41
	v_add3_u32 v2, v2, v5, s80
	ds_write_b16_d16_hi v54, v2 offset:54272
	v_mul_f32_e32 v2, v16, v40
	v_bfe_u32 v5, v2, 16, 1
	v_add3_u32 v2, v2, v5, s80
	ds_write_b16_d16_hi v54, v2 offset:54336
	v_mul_f32_e32 v2, v33, v41
	v_bfe_u32 v5, v2, 16, 1
	v_rcp_f32_e32 v42, v42
	v_add3_u32 v2, v2, v5, s80
	ds_write_b16_d16_hi v54, v2 offset:54400
	v_mul_f32_e32 v2, v17, v41
	v_bfe_u32 v5, v2, 16, 1
	v_add3_u32 v2, v2, v5, s80
	ds_write_b16_d16_hi v54, v2 offset:54464
	v_mul_f32_e32 v2, v34, v42
	v_bfe_u32 v5, v2, 16, 1
	v_rcp_f32_e32 v43, v43
	v_add3_u32 v2, v2, v5, s80
	ds_write_b16_d16_hi v54, v2 offset:54528
	v_mul_f32_e32 v2, v18, v42
	v_bfe_u32 v5, v2, 16, 1
	v_add3_u32 v2, v2, v5, s80
	ds_write_b16_d16_hi v54, v2 offset:54592
	v_mul_f32_e32 v2, v35, v43
	v_bfe_u32 v5, v2, 16, 1
	v_add3_u32 v2, v2, v5, s80
	ds_write_b16_d16_hi v4, v2 offset:54272
	v_mul_f32_e32 v2, v19, v43
	v_bfe_u32 v5, v2, 16, 1
	v_add3_u32 v2, v2, v5, s80
	ds_write_b16_d16_hi v4, v2 offset:54336
	v_lshlrev_b32_e32 v2, 3, v52
	v_and_b32_e32 v2, 56, v2
	s_waitcnt lgkmcnt(0)
	v_lshlrev_b32_e32 v6, 2, v2
	global_load_dwordx4 v[8:11], v6, s[30:31]
	global_load_dwordx4 v[12:15], v6, s[30:31] offset:16
	v_lshlrev_b32_e32 v2, 1, v2
	v_add_u32_e32 v7, s2, v2
	v_add_u32_e32 v4, v7, v53
	ds_read_b128 v[16:19], v4 offset:51200
	v_add_u32_e32 v24, 8, v36
	v_lshl_add_u32 v4, v24, 7, v7
	ds_read_b128 v[20:23], v4 offset:51200
	s_lshl_b64 s[2:3], s[14:15], 12
	s_waitcnt lgkmcnt(1)
	v_lshlrev_b32_e32 v27, 16, v17
	v_lshlrev_b32_e32 v26, 16, v16
	v_and_b32_e32 v17, 0xffff0000, v17
	v_and_b32_e32 v16, 0xffff0000, v16
	v_pk_mul_f32 v[4:5], v[26:27], v[26:27]
	v_pk_mul_f32 v[28:29], v[16:17], v[16:17]
	v_lshlrev_b32_e32 v30, 16, v18
	v_and_b32_e32 v18, 0xffff0000, v18
	v_add_f32_e32 v4, v4, v28
	v_mov_b32_e32 v32, v18
	v_mov_b32_e32 v33, v30
	v_add_f32_e32 v4, v5, v4
	v_lshlrev_b32_e32 v31, 16, v19
	v_and_b32_e32 v19, 0xffff0000, v19
	v_pk_mul_f32 v[32:33], v[32:33], v[32:33]
	v_add_f32_e32 v4, v29, v4
	v_mov_b32_e32 v34, v19
	v_mov_b32_e32 v35, v31
	v_add_f32_e32 v4, v33, v4
	v_pk_mul_f32 v[34:35], v[34:35], v[34:35]
	v_add_f32_e32 v4, v32, v4
	v_add_f32_e32 v4, v35, v4
	v_add_f32_e32 v4, v34, v4
	s_add_u32 s2, s22, s2
	s_addc_u32 s3, s23, s3
	v_add_f32_dpp v4, v4, v4 quad_perm:[1,0,3,2] row_mask:0xf bank_mask:0xf bound_ctrl:1
	v_ashrrev_i32_e32 v37, 31, v36
	s_nop 0
	v_add_f32_dpp v4, v4, v4 quad_perm:[2,3,0,1] row_mask:0xf bank_mask:0xf bound_ctrl:1
	s_nop 1
	v_add_f32_dpp v4, v4, v4 row_half_mirror row_mask:0xf bank_mask:0xf bound_ctrl:1
	v_fmamk_f32 v4, v4, 0x3c800000, v198
	v_mul_f32_e32 v5, 0x4f800000, v4
	v_cmp_gt_f32_e32 vcc, s82, v4
	s_nop 1
	v_cndmask_b32_e32 v25, v4, v5, vcc
	v_sqrt_f32_e32 v28, v25
	v_lshl_add_u64 v[4:5], s[2:3], 0, v[2:3]
	v_add_u32_e32 v2, -1, v28
	v_fma_f32 v29, -v2, v28, v25
	v_cmp_ge_f32_e64 s[2:3], 0, v29
	v_add_u32_e32 v29, 1, v28
	s_nop 0
	v_cndmask_b32_e64 v2, v28, v2, s[2:3]
	v_fma_f32 v28, -v29, v28, v25
	v_cmp_lt_f32_e64 s[2:3], 0, v28
	s_nop 1
	v_cndmask_b32_e64 v2, v2, v29, s[2:3]
	v_mul_f32_e32 v28, 0x37800000, v2
	v_cndmask_b32_e32 v2, v2, v28, vcc
	v_cmp_class_f32_e32 vcc, v25, v199
	s_waitcnt vmcnt(1)
	v_mov_b32_e32 v28, v8
	v_cndmask_b32_e32 v2, v2, v25, vcc
	v_div_scale_f32 v25, s[2:3], v2, v2, 1.0
	v_rcp_f32_e32 v32, v25
	v_mov_b32_e32 v29, v10
	v_mov_b32_e32 v10, v9
	v_fma_f32 v8, -v25, v32, 1.0
	v_fmac_f32_e32 v32, v8, v32
	v_div_scale_f32 v8, vcc, 1.0, v2, 1.0
	v_mul_f32_e32 v9, v8, v32
	v_fma_f32 v33, -v25, v9, v8
	v_fmac_f32_e32 v9, v33, v32
	v_fma_f32 v8, -v25, v9, v8
	v_div_fmas_f32 v8, v8, v32, v9
	v_div_fixup_f32 v2, v8, v2, 1.0
	v_pk_mul_f32 v[8:9], v[2:3], v[26:27] op_sel_hi:[0,1]
	v_pk_mul_f32 v[16:17], v[2:3], v[16:17] op_sel_hi:[0,1]
	s_waitcnt vmcnt(0)
	v_mov_b32_e32 v27, v14
	v_pk_mul_f32 v[18:19], v[2:3], v[18:19] op_sel_hi:[0,1]
	v_mov_b32_e32 v14, v13
	v_pk_mul_f32 v[10:11], v[10:11], v[16:17]
	v_pk_mul_f32 v[16:17], v[2:3], v[30:31] op_sel_hi:[0,1]
	v_mov_b32_e32 v26, v12
	v_pk_mul_f32 v[12:13], v[14:15], v[18:19]
	v_pk_mul_f32 v[16:17], v[26:27], v[16:17]
	v_bfe_u32 v2, v13, 16, 1
	v_pk_mul_f32 v[8:9], v[28:29], v[8:9]
	v_bfe_u32 v14, v12, 16, 1
	v_bfe_u32 v15, v11, 16, 1
	v_bfe_u32 v18, v10, 16, 1
	v_add3_u32 v2, v13, v2, s80
	v_bfe_u32 v13, v16, 16, 1
	v_add3_u32 v18, v10, v18, s80
	v_add3_u32 v15, v11, v15, s80
	v_add3_u32 v10, v12, v14, s80
	v_bfe_u32 v11, v8, 16, 1
	v_bfe_u32 v12, v9, 16, 1
	v_bfe_u32 v14, v17, 16, 1
	v_add3_u32 v13, v16, v13, s80
	v_add3_u32 v14, v17, v14, s80
	v_add3_u32 v9, v9, v12, s80
	v_add3_u32 v8, v8, v11, s80
	v_lshrrev_b32_e32 v12, 16, v13
	v_lshrrev_b32_e32 v8, 16, v8
	v_lshrrev_b32_e32 v9, 16, v9
	v_lshrrev_b32_e32 v11, 16, v14
	v_and_or_b32 v10, v10, s81, v12
	v_lshlrev_b64 v[12:13], 12, v[36:37]
	v_and_or_b32 v11, v2, s81, v11
	v_and_or_b32 v9, v15, s81, v9
	v_and_or_b32 v8, v18, s81, v8
	v_lshl_add_u64 v[12:13], v[4:5], 0, v[12:13]
	global_store_dwordx4 v[12:13], v[8:11], off
	global_load_dwordx4 v[8:11], v6, s[30:31]
	s_nop 0
	global_load_dwordx4 v[12:15], v6, s[30:31] offset:16
	s_waitcnt lgkmcnt(0)
	v_lshlrev_b32_e32 v17, 16, v21
	v_lshlrev_b32_e32 v16, 16, v20
	v_and_b32_e32 v19, 0xffff0000, v21
	v_and_b32_e32 v18, 0xffff0000, v20
	v_pk_mul_f32 v[20:21], v[16:17], v[16:17]
	v_pk_mul_f32 v[26:27], v[18:19], v[18:19]
	v_lshlrev_b32_e32 v28, 16, v22
	v_and_b32_e32 v22, 0xffff0000, v22
	v_add_f32_e32 v2, v20, v26
	v_mov_b32_e32 v30, v22
	v_mov_b32_e32 v31, v28
	v_add_f32_e32 v2, v21, v2
	v_lshlrev_b32_e32 v29, 16, v23
	v_and_b32_e32 v23, 0xffff0000, v23
	v_pk_mul_f32 v[30:31], v[30:31], v[30:31]
	v_add_f32_e32 v2, v27, v2
	v_mov_b32_e32 v32, v23
	v_mov_b32_e32 v33, v29
	v_add_f32_e32 v2, v31, v2
	v_pk_mul_f32 v[32:33], v[32:33], v[32:33]
	v_add_f32_e32 v2, v30, v2
	v_add_f32_e32 v2, v33, v2
	v_add_f32_e32 v2, v32, v2
	s_nop 1
	v_add_f32_dpp v2, v2, v2 quad_perm:[1,0,3,2] row_mask:0xf bank_mask:0xf bound_ctrl:1
	s_nop 1
	v_add_f32_dpp v2, v2, v2 quad_perm:[2,3,0,1] row_mask:0xf bank_mask:0xf bound_ctrl:1
	s_nop 1
	v_add_f32_dpp v2, v2, v2 row_half_mirror row_mask:0xf bank_mask:0xf bound_ctrl:1
	v_fmamk_f32 v2, v2, 0x3c800000, v198
	v_mul_f32_e32 v20, 0x4f800000, v2
	v_cmp_gt_f32_e32 vcc, s82, v2
	s_nop 1
	v_cndmask_b32_e32 v2, v2, v20, vcc
	v_sqrt_f32_e32 v20, v2
	s_nop 0
	v_add_u32_e32 v21, -1, v20
	v_fma_f32 v25, -v21, v20, v2
	v_cmp_ge_f32_e64 s[2:3], 0, v25
	v_add_u32_e32 v25, 1, v20
	s_nop 0
	v_cndmask_b32_e64 v21, v20, v21, s[2:3]
	v_fma_f32 v20, -v25, v20, v2
	v_cmp_lt_f32_e64 s[2:3], 0, v20
	s_nop 1
	v_cndmask_b32_e64 v20, v21, v25, s[2:3]
	v_mul_f32_e32 v21, 0x37800000, v20
	v_cndmask_b32_e32 v20, v20, v21, vcc
	v_cmp_class_f32_e32 vcc, v2, v199
	s_waitcnt vmcnt(1)
	v_mov_b32_e32 v21, v10
	v_cndmask_b32_e32 v2, v20, v2, vcc
	v_div_scale_f32 v25, s[2:3], v2, v2, 1.0
	v_rcp_f32_e32 v26, v25
	v_mov_b32_e32 v20, v8
	v_mov_b32_e32 v10, v9
	v_fma_f32 v8, -v25, v26, 1.0
	v_fmac_f32_e32 v26, v8, v26
	v_div_scale_f32 v8, vcc, 1.0, v2, 1.0
	v_mul_f32_e32 v9, v8, v26
	v_fma_f32 v27, -v25, v9, v8
	v_fmac_f32_e32 v9, v27, v26
	v_fma_f32 v8, -v25, v9, v8
	v_div_fmas_f32 v8, v8, v26, v9
	v_div_fixup_f32 v2, v8, v2, 1.0
	v_pk_mul_f32 v[8:9], v[2:3], v[16:17] op_sel_hi:[0,1]
	v_pk_mul_f32 v[16:17], v[2:3], v[18:19] op_sel_hi:[0,1]
	v_pk_mul_f32 v[10:11], v[10:11], v[16:17]
	v_pk_mul_f32 v[16:17], v[2:3], v[28:29] op_sel_hi:[0,1]
	s_waitcnt vmcnt(0)
	v_mov_b32_e32 v18, v12
	v_mov_b32_e32 v19, v14
	v_pk_mul_f32 v[16:17], v[18:19], v[16:17]
	v_pk_mul_f32 v[18:19], v[2:3], v[22:23] op_sel_hi:[0,1]
	v_mov_b32_e32 v14, v13
	v_pk_mul_f32 v[12:13], v[14:15], v[18:19]
	v_pk_mul_f32 v[8:9], v[20:21], v[8:9]
	v_bfe_u32 v2, v13, 16, 1
	v_bfe_u32 v14, v12, 16, 1
	v_bfe_u32 v15, v11, 16, 1
	v_bfe_u32 v18, v10, 16, 1
	v_add3_u32 v2, v13, v2, s80
	v_bfe_u32 v13, v16, 16, 1
	v_add3_u32 v18, v10, v18, s80
	v_add3_u32 v15, v11, v15, s80
	v_add3_u32 v10, v12, v14, s80
	v_bfe_u32 v11, v8, 16, 1
	v_bfe_u32 v12, v9, 16, 1
	v_bfe_u32 v14, v17, 16, 1
	v_add3_u32 v13, v16, v13, s80
	v_add3_u32 v14, v17, v14, s80
	v_add3_u32 v9, v9, v12, s80
	v_add3_u32 v8, v8, v11, s80
	v_lshrrev_b32_e32 v12, 16, v13
	v_ashrrev_i32_e32 v25, 31, v24
	v_lshrrev_b32_e32 v8, 16, v8
	v_lshrrev_b32_e32 v9, 16, v9
	v_lshrrev_b32_e32 v11, 16, v14
	v_and_or_b32 v10, v10, s81, v12
	v_lshlrev_b64 v[12:13], 12, v[24:25]
	v_and_or_b32 v11, v2, s81, v11
	v_and_or_b32 v9, v15, s81, v9
	v_and_or_b32 v8, v18, s81, v8
	v_lshl_add_u64 v[12:13], v[4:5], 0, v[12:13]
	global_store_dwordx4 v[12:13], v[8:11], off
	global_load_dwordx4 v[8:11], v6, s[30:31]
	s_nop 0
	global_load_dwordx4 v[12:15], v6, s[30:31] offset:16
	v_add_u32_e32 v24, 16, v36
	v_lshl_add_u32 v2, v24, 7, v7
	ds_read_b128 v[16:19], v2 offset:51200
	v_add_u32_e32 v26, 24, v36
	v_lshl_add_u32 v2, v26, 7, v7
	ds_read_b128 v[20:23], v2 offset:51200
	s_waitcnt lgkmcnt(1)
	v_lshlrev_b32_e32 v29, 16, v17
	v_lshlrev_b32_e32 v28, 16, v16
	v_and_b32_e32 v17, 0xffff0000, v17
	v_and_b32_e32 v16, 0xffff0000, v16
	v_pk_mul_f32 v[30:31], v[28:29], v[28:29]
	v_pk_mul_f32 v[32:33], v[16:17], v[16:17]
	v_lshlrev_b32_e32 v34, 16, v18
	v_and_b32_e32 v18, 0xffff0000, v18
	v_add_f32_e32 v2, v30, v32
	v_mov_b32_e32 v36, v18
	v_mov_b32_e32 v37, v34
	v_add_f32_e32 v2, v31, v2
	v_lshlrev_b32_e32 v35, 16, v19
	v_and_b32_e32 v19, 0xffff0000, v19
	v_pk_mul_f32 v[36:37], v[36:37], v[36:37]
	v_add_f32_e32 v2, v33, v2
	v_mov_b32_e32 v38, v19
	v_mov_b32_e32 v39, v35
	v_add_f32_e32 v2, v37, v2
	v_pk_mul_f32 v[38:39], v[38:39], v[38:39]
	v_add_f32_e32 v2, v36, v2
	v_add_f32_e32 v2, v39, v2
	v_add_f32_e32 v2, v38, v2
	s_waitcnt vmcnt(1)
	v_mov_b32_e32 v30, v8
	v_add_f32_dpp v2, v2, v2 quad_perm:[1,0,3,2] row_mask:0xf bank_mask:0xf bound_ctrl:1
	v_mov_b32_e32 v31, v10
	v_mov_b32_e32 v10, v9
	v_add_f32_dpp v2, v2, v2 quad_perm:[2,3,0,1] row_mask:0xf bank_mask:0xf bound_ctrl:1
	s_nop 1
	v_add_f32_dpp v2, v2, v2 row_half_mirror row_mask:0xf bank_mask:0xf bound_ctrl:1
	v_fmamk_f32 v2, v2, 0x3c800000, v198
	v_mul_f32_e32 v7, 0x4f800000, v2
	v_cmp_gt_f32_e32 vcc, s82, v2
	s_nop 1
	v_cndmask_b32_e32 v2, v2, v7, vcc
	v_sqrt_f32_e32 v7, v2
	s_nop 0
	v_add_u32_e32 v25, -1, v7
	v_fma_f32 v27, -v25, v7, v2
	v_cmp_ge_f32_e64 s[2:3], 0, v27
	v_add_u32_e32 v27, 1, v7
	s_nop 0
	v_cndmask_b32_e64 v25, v7, v25, s[2:3]
	v_fma_f32 v7, -v27, v7, v2
	v_cmp_lt_f32_e64 s[2:3], 0, v7
	s_nop 1
	v_cndmask_b32_e64 v7, v25, v27, s[2:3]
	v_mul_f32_e32 v25, 0x37800000, v7
	v_cndmask_b32_e32 v7, v7, v25, vcc
	v_cmp_class_f32_e32 vcc, v2, v199
	s_nop 1
	v_cndmask_b32_e32 v2, v7, v2, vcc
	v_div_scale_f32 v7, s[2:3], v2, v2, 1.0
	v_rcp_f32_e32 v25, v7
	s_nop 0
	v_fma_f32 v8, -v7, v25, 1.0
	v_fmac_f32_e32 v25, v8, v25
	v_div_scale_f32 v8, vcc, 1.0, v2, 1.0
	v_mul_f32_e32 v9, v8, v25
	v_fma_f32 v27, -v7, v9, v8
	v_fmac_f32_e32 v9, v27, v25
	v_fma_f32 v7, -v7, v9, v8
	v_div_fmas_f32 v7, v7, v25, v9
	v_div_fixup_f32 v2, v7, v2, 1.0
	v_pk_mul_f32 v[8:9], v[2:3], v[28:29] op_sel_hi:[0,1]
	v_pk_mul_f32 v[16:17], v[2:3], v[16:17] op_sel_hi:[0,1]
	s_waitcnt vmcnt(0)
	v_mov_b32_e32 v29, v14
	v_pk_mul_f32 v[18:19], v[2:3], v[18:19] op_sel_hi:[0,1]
	v_mov_b32_e32 v14, v13
	v_pk_mul_f32 v[10:11], v[10:11], v[16:17]
	v_pk_mul_f32 v[16:17], v[2:3], v[34:35] op_sel_hi:[0,1]
	v_mov_b32_e32 v28, v12
	v_pk_mul_f32 v[12:13], v[14:15], v[18:19]
	v_pk_mul_f32 v[8:9], v[30:31], v[8:9]
	v_pk_mul_f32 v[16:17], v[28:29], v[16:17]
	v_bfe_u32 v2, v13, 16, 1
	v_bfe_u32 v7, v12, 16, 1
	v_bfe_u32 v14, v11, 16, 1
	v_bfe_u32 v15, v10, 16, 1
	v_add3_u32 v15, v10, v15, s80
	v_add3_u32 v14, v11, v14, s80
	v_add3_u32 v7, v12, v7, s80
	v_add3_u32 v2, v13, v2, s80
	v_bfe_u32 v10, v8, 16, 1
	v_bfe_u32 v11, v9, 16, 1
	v_bfe_u32 v12, v16, 16, 1
	v_bfe_u32 v13, v17, 16, 1
	v_add3_u32 v13, v17, v13, s80
	v_add3_u32 v12, v16, v12, s80
	v_add3_u32 v9, v9, v11, s80
	v_add3_u32 v8, v8, v10, s80
	v_ashrrev_i32_e32 v25, 31, v24
	v_lshrrev_b32_e32 v8, 16, v8
	v_lshrrev_b32_e32 v9, 16, v9
	v_lshrrev_b32_e32 v10, 16, v12
	v_lshrrev_b32_e32 v11, 16, v13
	v_lshlrev_b64 v[12:13], 12, v[24:25]
	v_and_or_b32 v11, v2, s81, v11
	v_and_or_b32 v10, v7, s81, v10
	v_and_or_b32 v9, v14, s81, v9
	v_and_or_b32 v8, v15, s81, v8
	v_lshl_add_u64 v[12:13], v[4:5], 0, v[12:13]
	global_store_dwordx4 v[12:13], v[8:11], off
	global_load_dwordx4 v[8:11], v6, s[30:31]
	s_nop 0
	global_load_dwordx4 v[12:15], v6, s[30:31] offset:16
	s_waitcnt lgkmcnt(0)
	v_lshlrev_b32_e32 v7, 16, v21
	v_lshlrev_b32_e32 v6, 16, v20
	v_and_b32_e32 v17, 0xffff0000, v21
	v_and_b32_e32 v16, 0xffff0000, v20
	v_pk_mul_f32 v[18:19], v[6:7], v[6:7]
	v_pk_mul_f32 v[20:21], v[16:17], v[16:17]
	v_lshlrev_b32_e32 v24, 16, v22
	v_and_b32_e32 v22, 0xffff0000, v22
	v_add_f32_e32 v2, v18, v20
	v_mov_b32_e32 v28, v22
	v_mov_b32_e32 v29, v24
	v_add_f32_e32 v2, v19, v2
	v_lshlrev_b32_e32 v25, 16, v23
	v_and_b32_e32 v23, 0xffff0000, v23
	v_pk_mul_f32 v[28:29], v[28:29], v[28:29]
	v_add_f32_e32 v2, v21, v2
	v_mov_b32_e32 v30, v23
	v_mov_b32_e32 v31, v25
	v_add_f32_e32 v2, v29, v2
	v_pk_mul_f32 v[30:31], v[30:31], v[30:31]
	v_add_f32_e32 v2, v28, v2
	v_add_f32_e32 v2, v31, v2
	v_add_f32_e32 v2, v30, v2
	s_nop 1
	v_add_f32_dpp v2, v2, v2 quad_perm:[1,0,3,2] row_mask:0xf bank_mask:0xf bound_ctrl:1
	s_nop 1
	v_add_f32_dpp v2, v2, v2 quad_perm:[2,3,0,1] row_mask:0xf bank_mask:0xf bound_ctrl:1
	s_nop 1
	v_add_f32_dpp v2, v2, v2 row_half_mirror row_mask:0xf bank_mask:0xf bound_ctrl:1
	v_fmamk_f32 v2, v2, 0x3c800000, v198
	v_mul_f32_e32 v18, 0x4f800000, v2
	v_cmp_gt_f32_e32 vcc, s82, v2
	s_nop 1
	v_cndmask_b32_e32 v2, v2, v18, vcc
	v_sqrt_f32_e32 v18, v2
	s_nop 0
	v_add_u32_e32 v19, -1, v18
	v_fma_f32 v20, -v19, v18, v2
	v_cmp_ge_f32_e64 s[2:3], 0, v20
	v_add_u32_e32 v20, 1, v18
	s_nop 0
	v_cndmask_b32_e64 v19, v18, v19, s[2:3]
	v_fma_f32 v18, -v20, v18, v2
	v_cmp_lt_f32_e64 s[2:3], 0, v18
	s_nop 1
	v_cndmask_b32_e64 v18, v19, v20, s[2:3]
	v_mul_f32_e32 v19, 0x37800000, v18
	v_cndmask_b32_e32 v18, v18, v19, vcc
	v_cmp_class_f32_e32 vcc, v2, v199
	s_waitcnt vmcnt(1)
	v_mov_b32_e32 v19, v10
	v_cndmask_b32_e32 v2, v18, v2, vcc
	v_div_scale_f32 v20, s[2:3], v2, v2, 1.0
	v_rcp_f32_e32 v21, v20
	v_mov_b32_e32 v18, v8
	v_mov_b32_e32 v10, v9
	s_and_b64 s[2:3], s[12:13], s[58:59]
	v_fma_f32 v8, -v20, v21, 1.0
	v_fmac_f32_e32 v21, v8, v21
	v_div_scale_f32 v8, vcc, 1.0, v2, 1.0
	v_mul_f32_e32 v9, v8, v21
	v_fma_f32 v27, -v20, v9, v8
	v_fmac_f32_e32 v9, v27, v21
	v_fma_f32 v8, -v20, v9, v8
	v_div_fmas_f32 v8, v8, v21, v9
	v_div_fixup_f32 v2, v8, v2, 1.0
	v_pk_mul_f32 v[8:9], v[2:3], v[16:17] op_sel_hi:[0,1]
	v_pk_mul_f32 v[8:9], v[10:11], v[8:9]
	v_pk_mul_f32 v[10:11], v[2:3], v[24:25] op_sel_hi:[0,1]
	s_waitcnt vmcnt(0)
	v_mov_b32_e32 v16, v12
	v_mov_b32_e32 v17, v14
	v_pk_mul_f32 v[10:11], v[16:17], v[10:11]
	v_pk_mul_f32 v[16:17], v[2:3], v[22:23] op_sel_hi:[0,1]
	v_mov_b32_e32 v14, v13
	v_pk_mul_f32 v[12:13], v[14:15], v[16:17]
	v_pk_mul_f32 v[6:7], v[2:3], v[6:7] op_sel_hi:[0,1]
	v_bfe_u32 v2, v13, 16, 1
	v_pk_mul_f32 v[6:7], v[18:19], v[6:7]
	v_bfe_u32 v14, v12, 16, 1
	v_bfe_u32 v15, v9, 16, 1
	v_bfe_u32 v16, v8, 16, 1
	v_add3_u32 v2, v13, v2, s80
	v_bfe_u32 v13, v10, 16, 1
	v_add3_u32 v16, v8, v16, s80
	v_add3_u32 v15, v9, v15, s80
	v_add3_u32 v8, v12, v14, s80
	v_bfe_u32 v9, v6, 16, 1
	v_bfe_u32 v12, v7, 16, 1
	v_bfe_u32 v14, v11, 16, 1
	v_add3_u32 v10, v10, v13, s80
	v_add3_u32 v11, v11, v14, s80
	v_add3_u32 v7, v7, v12, s80
	v_add3_u32 v6, v6, v9, s80
	v_lshrrev_b32_e32 v10, 16, v10
	v_ashrrev_i32_e32 v27, 31, v26
	v_lshrrev_b32_e32 v6, 16, v6
	v_lshrrev_b32_e32 v7, 16, v7
	v_lshrrev_b32_e32 v9, 16, v11
	v_and_or_b32 v8, v8, s81, v10
	v_lshlrev_b64 v[10:11], 12, v[26:27]
	v_and_or_b32 v9, v2, s81, v9
	v_and_or_b32 v7, v15, s81, v7
	v_and_or_b32 v6, v16, s81, v6
	v_lshl_add_u64 v[4:5], v[4:5], 0, v[10:11]
	global_store_dwordx4 v[4:5], v[6:9], off
	s_waitcnt lgkmcnt(0)
	s_barrier
	s_andn2_b64 vcc, exec, s[2:3]
	s_cbranch_vccnz .LBB0_300
	v_writelane_b32 v255, 5, 5
	v_writelane_b32 v255, 12, 6
	s_branch .Lmy_cvgu

.LBB0_514:
	v_readlane_b32 s70, v252, 7
	s_cmp_eq_u32 s70, 3
	s_cbranch_scc0 .LBB0_519
	v_readlane_b32 s58, v252, 9
	v_writelane_b32 v255, 7, 5
	v_writelane_b32 v255, 12, 6
	s_branch .Lmy_cvgu
